# static s_setprio 1 for waves 4-7 during MIX attention phase
# speedup vs baseline: 1.0047x; 1.0047x over previous
.LBB0_648:
	v_writelane_b32 v254, s30, 62
	v_writelane_b32 v254, s50, 63
	s_nop 1
	v_writelane_b32 v255, s51, 0
	s_or_b64 exec, exec, s[4:5]
	v_readlane_b32 s4, v253, 0
	v_readlane_b32 s5, v253, 1
	s_waitcnt lgkmcnt(0)
	s_barrier
	s_getreg_b32 s98, hwreg(HW_REG_HW_ID, 0, 6)
	s_and_b32 s98, s98, 63
	s_lshl_b32 s98, s98, 2
	s_add_i32 s98, s98, 0x20010
	v_mov_b32_e32 v0, s98
	ds_read_b32 v0, v0
	s_waitcnt lgkmcnt(0)
	v_readfirstlane_b32 s98, v0
	s_cmp_ge_u32 s98, 4
	s_cbranch_scc0 .Lmixprio_skip
	s_setprio 1
.Lmixprio_skip:
	s_load_dwordx2 s[46:47], s[4:5], 0x58
	s_load_dwordx2 s[6:7], s[4:5], 0x68
	v_readlane_b32 s0, v254, 54
	s_load_dwordx2 s[96:97], s[4:5], 0xf0
	s_waitcnt lgkmcnt(0)
	v_writelane_b32 v255, s6, 1
	s_nop 1
	v_writelane_b32 v255, s7, 2
	s_load_dwordx2 s[6:7], s[4:5], 0x78
	s_add_u32 s4, s96, 0x13100000
	s_addc_u32 s5, s97, 0
	s_add_u32 s0, s96, 0x17000000
	s_waitcnt lgkmcnt(0)
	v_writelane_b32 v255, s6, 3
	s_nop 1
	v_writelane_b32 v255, s7, 4
	v_writelane_b32 v255, s4, 5
	s_nop 1
	v_writelane_b32 v255, s5, 6
	v_writelane_b32 v255, s0, 7
	s_addc_u32 s0, s97, 0
	v_writelane_b32 v255, s0, 8
	s_add_u32 s0, s96, 0x14c00000
	v_readlane_b32 s4, v253, 6
	v_writelane_b32 v255, s0, 9
	s_addc_u32 s0, s97, 0
	v_readlane_b32 s5, v253, 7
	v_writelane_b32 v255, s0, 10
	s_andn2_b64 vcc, exec, s[4:5]
	s_cbranch_vccnz .LBB0_668
	s_add_u32 s14, s96, 0x18818000
	s_addc_u32 s15, s97, 0
	s_add_u32 s16, s96, 0x16c20100
	s_addc_u32 s17, s97, 0
	s_mov_b32 s18, s76
	s_mov_b32 s19, s76
	s_branch .LBB0_651

.LBB0_993:
	s_setprio 0
	s_waitcnt vmcnt(0)
	s_barrier
	s_getreg_b32 s0, hwreg(HW_REG_HW_ID, 0, 6)
	s_and_b32 s0, s0, 63
	s_lshl_b32 s0, s0, 2
	s_add_i32 s0, s0, 0
	s_add_i32 s0, s0, 0x20010
	v_mov_b32_e32 v0, s0
	ds_read_b32 v0, v0
	s_waitcnt lgkmcnt(0)
	v_readfirstlane_b32 s0, v0
	v_mbcnt_lo_u32_b32 v0, -1, 0
	v_mbcnt_hi_u32_b32 v0, -1, v0
	s_nop 1
	v_lshl_or_b32 v0, s0, 6, v0
	v_cmp_eq_u32_e32 vcc, 0, v0
	s_and_saveexec_b64 s[4:5], vcc
	v_readlane_b32 s76, v254, 47
	v_readlane_b32 s80, v254, 49
	v_readlane_b32 s77, v254, 48
	v_readlane_b32 s81, v254, 50
	s_movk_i32 s65, 0x110
	s_cbranch_execz .LBB0_1345
	s_add_i32 s2, 0, 0x20000
	v_mov_b32_e32 v0, s2
	s_getreg_b32 s0, hwreg(HW_REG_XCC_ID, 0, 4)
	s_waitcnt vmcnt(0) expcnt(0) lgkmcnt(0)
	ds_read_b32 v2, v0
	v_readlane_b32 s6, v254, 29
	s_and_b32 s0, s0, 15
	s_waitcnt lgkmcnt(0)
	v_cmp_ne_u32_e32 vcc, 0, v2
	v_mov_b32_e32 v0, s6
	ds_read_b32 v0, v0
	s_cbranch_vccnz .LBB0_1309
	v_readlane_b32 s8, v253, 4
	v_readlane_b32 s9, v253, 5
	s_load_dwordx2 s[6:7], s[8:9], 0x4
	s_mov_b32 s13, 1
	s_waitcnt lgkmcnt(0)
	s_mul_i32 s12, s6, s80
	s_mul_i32 s12, s12, s7
	s_branch .LBB0_1297
